# merge-GEMM epilogue: the 32 serial gate loads are issued together into dead fragment registers, one wait
# speedup vs baseline: 1.0377x; 1.0005x over previous
.LBB0_1679:
	v_mbcnt_lo_u32_b32 v1, -1, 0
	v_mbcnt_hi_u32_b32 v1, -1, v1
	s_ashr_i32 s1, s0, 31
	v_and_or_b32 v2, v1, 15, s59
	v_ashrrev_i32_e32 v1, 1, v1
	v_and_b32_e32 v4, -8, v1
	s_lshl_b64 s[0:1], s[0:1], 19
	v_ashrrev_i32_e32 v5, 31, v4
	s_or_b64 s[0:1], s[0:1], s[2:3]
	v_lshlrev_b64 v[38:39], 11, v[2:3]
	v_lshl_add_u64 v[4:5], s[0:1], 0, v[4:5]
	s_lshl_b32 s42, s46, 8
	v_lshl_add_u64 v[4:5], v[4:5], 0, v[38:39]
	s_ashr_i32 s43, s42, 31
	v_lshl_add_u64 v[70:71], v[4:5], 0, s[42:43]
	global_load_dwordx2 v[174:175], v70, s[10:11]
	global_load_dwordx2 v[176:177], v70, s[10:11] offset:128
	global_load_dwordx2 v[178:179], v70, s[8:9]
	global_load_dwordx2 v[180:181], v70, s[8:9] offset:128
	v_add_u32_e32 v252, 0x8000, v70
	global_load_dwordx2 v[182:183], v252, s[10:11]
	global_load_dwordx2 v[184:185], v252, s[10:11] offset:128
	global_load_dwordx2 v[186:187], v252, s[8:9]
	global_load_dwordx2 v[188:189], v252, s[8:9] offset:128
	v_add_u32_e32 v252, 0x10000, v70
	global_load_dwordx2 v[190:191], v252, s[10:11]
	global_load_dwordx2 v[192:193], v252, s[10:11] offset:128
	global_load_dwordx2 v[194:195], v252, s[8:9]
	global_load_dwordx2 v[196:197], v252, s[8:9] offset:128
	v_add_u32_e32 v252, 0x18000, v70
	global_load_dwordx2 v[198:199], v252, s[10:11]
	global_load_dwordx2 v[200:201], v252, s[10:11] offset:128
	global_load_dwordx2 v[202:203], v252, s[8:9]
	global_load_dwordx2 v[204:205], v252, s[8:9] offset:128
	v_add_u32_e32 v252, 0x40000, v70
	global_load_dwordx2 v[206:207], v252, s[10:11]
	global_load_dwordx2 v[208:209], v252, s[10:11] offset:128
	global_load_dwordx2 v[210:211], v252, s[8:9]
	global_load_dwordx2 v[212:213], v252, s[8:9] offset:128
	v_add_u32_e32 v252, 0x48000, v70
	global_load_dwordx2 v[214:215], v252, s[10:11]
	global_load_dwordx2 v[216:217], v252, s[10:11] offset:128
	global_load_dwordx2 v[218:219], v252, s[8:9]
	global_load_dwordx2 v[220:221], v252, s[8:9] offset:128
	v_add_u32_e32 v252, 0x50000, v70
	global_load_dwordx2 v[222:223], v252, s[10:11]
	global_load_dwordx2 v[224:225], v252, s[10:11] offset:128
	global_load_dwordx2 v[226:227], v252, s[8:9]
	global_load_dwordx2 v[228:229], v252, s[8:9] offset:128
	v_add_u32_e32 v252, 0x58000, v70
	global_load_dwordx2 v[230:231], v252, s[10:11]
	global_load_dwordx2 v[232:233], v252, s[10:11] offset:128
	global_load_dwordx2 v[234:235], v252, s[8:9]
	global_load_dwordx2 v[236:237], v252, s[8:9] offset:128
	v_lshl_add_u64 v[38:39], s[10:11], 0, v[70:71]
	s_cmp_eq_u32 s47, 0
	s_cselect_b64 s[40:41], -1, 0
	s_cmp_lg_u32 s47, 0
	s_mov_b64 s[0:1], -1
	s_cselect_b64 s[46:47], -1, 0
	s_and_b64 vcc, exec, s[40:41]
	s_waitcnt vmcnt(0)
	v_mov_b32_e32 v72, v174
	v_mov_b32_e32 v73, v175
	v_cvt_f32_ubyte0_e32 v1, v72
	v_cvt_f32_ubyte0_e32 v2, v73
	v_cvt_f32_ubyte1_e32 v74, v72
	v_cvt_f32_ubyte1_e32 v75, v73
	v_cvt_f32_ubyte2_e32 v76, v72
	v_cvt_f32_ubyte2_e32 v77, v73
	v_cvt_f32_ubyte3_e32 v72, v72
	v_cvt_f32_ubyte3_e32 v73, v73
	v_mul_f32_e32 v1, 0x3b808081, v1
	v_mul_f32_e32 v2, 0x3b808081, v2
	v_mul_f32_e32 v74, 0x3b808081, v74
	v_mul_f32_e32 v103, 0x3b808081, v75
	v_mul_f32_e32 v76, 0x3b808081, v76
	v_mul_f32_e32 v104, 0x3b808081, v77
	v_mul_f32_e32 v72, 0x3b808081, v72
	v_mul_f32_e32 v105, 0x3b808081, v73
	v_max_f32_e32 v77, 0x1e3ce508, v1
	v_max_f32_e32 v75, 0x1e3ce508, v74
	v_max_f32_e32 v73, 0x1e3ce508, v76
	v_max_f32_e32 v72, 0x1e3ce508, v72
	v_max_f32_e32 v102, 0x1e3ce508, v2
	v_max_f32_e32 v76, 0x1e3ce508, v103
	v_max_f32_e32 v74, 0x1e3ce508, v104
	v_max_f32_e32 v2, 0x1e3ce508, v105
	s_cbranch_vccnz .LBB0_1681
	v_lshl_add_u64 v[38:39], s[8:9], 0, v[70:71]
	v_mov_b32_e32 v38, v178
	v_mov_b32_e32 v39, v179
	v_rcp_f32_e32 v1, v77
	v_rcp_f32_e32 v40, v102
	v_rcp_f32_e32 v41, v75
	v_rcp_f32_e32 v42, v76
	v_rcp_f32_e32 v43, v73
	v_rcp_f32_e32 v44, v74
	v_rcp_f32_e32 v45, v72
	v_rcp_f32_e32 v103, v2
	s_mov_b64 s[0:1], 0
	v_cvt_f32_ubyte0_e32 v104, v38
	v_cvt_f32_ubyte0_e32 v105, v39
	v_cvt_f32_ubyte1_e32 v106, v38
	v_cvt_f32_ubyte1_e32 v107, v39
	v_cvt_f32_ubyte2_e32 v108, v38
	v_cvt_f32_ubyte2_e32 v109, v39
	v_cvt_f32_ubyte3_e32 v38, v38
	v_cvt_f32_ubyte3_e32 v39, v39
	v_mul_f32_e32 v104, 0x3b808081, v104
	v_mul_f32_e32 v105, 0x3b808081, v105
	v_mul_f32_e32 v106, 0x3b808081, v106
	v_mul_f32_e32 v107, 0x3b808081, v107
	v_mul_f32_e32 v108, 0x3b808081, v108
	v_mul_f32_e32 v109, 0x3b808081, v109
	v_mul_f32_e32 v38, 0x3b808081, v38
	v_mul_f32_e32 v39, 0x3b808081, v39
	v_mul_f32_e32 v1, v1, v104
	v_mul_f32_e32 v40, v40, v105
	v_mul_f32_e32 v41, v41, v106
	v_mul_f32_e32 v104, v42, v107
	v_mul_f32_e32 v105, v43, v108
	v_mul_f32_e32 v44, v44, v109
	v_mul_f32_e32 v45, v45, v38
	v_mul_f32_e32 v103, v103, v39
	v_mul_f32_e32 v38, v58, v1
	v_mul_f32_e32 v42, v54, v40
	v_mul_f32_e32 v39, v59, v41
	v_mul_f32_e32 v43, v55, v104
	v_mul_f32_e32 v40, v60, v105
	v_mul_f32_e32 v44, v56, v44
	v_mul_f32_e32 v41, v61, v45
	v_mul_f32_e32 v45, v57, v103

.LBB0_1683:
	s_or_b32 s44, s42, 0x80
	s_mov_b32 s45, s43
	v_lshl_add_u64 v[70:71], v[4:5], 0, s[44:45]
	v_lshl_add_u64 v[54:55], s[10:11], 0, v[70:71]
	v_mov_b32_e32 v54, v176
	v_mov_b32_e32 v55, v177
	v_cndmask_b32_e64 v1, 0, 1, s[46:47]
	v_cmp_ne_u32_e64 s[0:1], 1, v1
	s_andn2_b64 vcc, exec, s[46:47]
	s_mov_b64 s[46:47], -1
	v_cvt_f32_ubyte0_e32 v1, v54
	v_cvt_f32_ubyte0_e32 v2, v55
	v_cvt_f32_ubyte1_e32 v56, v54
	v_cvt_f32_ubyte1_e32 v57, v55
	v_cvt_f32_ubyte2_e32 v58, v54
	v_cvt_f32_ubyte2_e32 v59, v55
	v_cvt_f32_ubyte3_e32 v54, v54
	v_cvt_f32_ubyte3_e32 v55, v55
	v_mul_f32_e32 v1, 0x3b808081, v1
	v_mul_f32_e32 v2, 0x3b808081, v2
	v_mul_f32_e32 v56, 0x3b808081, v56
	v_mul_f32_e32 v57, 0x3b808081, v57
	v_mul_f32_e32 v58, 0x3b808081, v58
	v_mul_f32_e32 v59, 0x3b808081, v59
	v_mul_f32_e32 v54, 0x3b808081, v54
	v_mul_f32_e32 v55, 0x3b808081, v55
	v_max_f32_e32 v77, 0x1e3ce508, v1
	v_max_f32_e32 v75, 0x1e3ce508, v56
	v_max_f32_e32 v73, 0x1e3ce508, v58
	v_max_f32_e32 v72, 0x1e3ce508, v54
	v_max_f32_e32 v102, 0x1e3ce508, v2
	v_max_f32_e32 v76, 0x1e3ce508, v57
	v_max_f32_e32 v74, 0x1e3ce508, v59
	v_max_f32_e32 v2, 0x1e3ce508, v55
	s_cbranch_vccnz .LBB0_1685
	v_lshl_add_u64 v[54:55], s[8:9], 0, v[70:71]
	v_mov_b32_e32 v54, v180
	v_mov_b32_e32 v55, v181
	v_rcp_f32_e32 v1, v77
	v_rcp_f32_e32 v56, v102
	v_rcp_f32_e32 v57, v75
	v_rcp_f32_e32 v58, v76
	v_rcp_f32_e32 v59, v73
	v_rcp_f32_e32 v60, v74
	v_rcp_f32_e32 v61, v72
	v_rcp_f32_e32 v103, v2
	s_mov_b64 s[46:47], 0
	v_cvt_f32_ubyte0_e32 v104, v54
	v_cvt_f32_ubyte0_e32 v105, v55
	v_cvt_f32_ubyte1_e32 v106, v54
	v_cvt_f32_ubyte1_e32 v107, v55
	v_cvt_f32_ubyte2_e32 v108, v54
	v_cvt_f32_ubyte2_e32 v109, v55
	v_cvt_f32_ubyte3_e32 v54, v54
	v_cvt_f32_ubyte3_e32 v55, v55
	v_mul_f32_e32 v104, 0x3b808081, v104
	v_mul_f32_e32 v105, 0x3b808081, v105
	v_mul_f32_e32 v106, 0x3b808081, v106
	v_mul_f32_e32 v107, 0x3b808081, v107
	v_mul_f32_e32 v108, 0x3b808081, v108
	v_mul_f32_e32 v109, 0x3b808081, v109
	v_mul_f32_e32 v54, 0x3b808081, v54
	v_mul_f32_e32 v55, 0x3b808081, v55
	v_mul_f32_e32 v1, v1, v104
	v_mul_f32_e32 v56, v56, v105
	v_mul_f32_e32 v57, v57, v106
	v_mul_f32_e32 v104, v58, v107
	v_mul_f32_e32 v105, v59, v108
	v_mul_f32_e32 v60, v60, v109
	v_mul_f32_e32 v61, v61, v54
	v_mul_f32_e32 v103, v103, v55
	v_mul_f32_e32 v54, v162, v1
	v_mul_f32_e32 v58, v158, v56
	v_mul_f32_e32 v55, v163, v57
	v_mul_f32_e32 v59, v159, v104
	v_mul_f32_e32 v56, v164, v105
	v_mul_f32_e32 v60, v160, v60
	v_mul_f32_e32 v57, v165, v61
	v_mul_f32_e32 v61, v161, v103

.LBB0_1687:
	v_lshl_add_u64 v[102:103], v[4:5], 0, s[18:19]
	v_lshl_add_u64 v[104:105], v[102:103], 0, s[42:43]
	v_lshl_add_u64 v[70:71], s[10:11], 0, v[104:105]
	v_mov_b32_e32 v70, v182
	v_mov_b32_e32 v71, v183
	s_and_b64 vcc, exec, s[0:1]
	s_mov_b64 s[46:47], -1
	v_cvt_f32_ubyte0_e32 v1, v70
	v_cvt_f32_ubyte0_e32 v2, v71
	v_cvt_f32_ubyte1_e32 v72, v70
	v_cvt_f32_ubyte1_e32 v73, v71
	v_cvt_f32_ubyte2_e32 v74, v70
	v_cvt_f32_ubyte2_e32 v75, v71
	v_cvt_f32_ubyte3_e32 v70, v70
	v_cvt_f32_ubyte3_e32 v71, v71
	v_mul_f32_e32 v1, 0x3b808081, v1
	v_mul_f32_e32 v2, 0x3b808081, v2
	v_mul_f32_e32 v72, 0x3b808081, v72
	v_mul_f32_e32 v73, 0x3b808081, v73
	v_mul_f32_e32 v74, 0x3b808081, v74
	v_mul_f32_e32 v75, 0x3b808081, v75
	v_mul_f32_e32 v70, 0x3b808081, v70
	v_mul_f32_e32 v71, 0x3b808081, v71
	v_max_f32_e32 v135, 0x1e3ce508, v1
	v_max_f32_e32 v109, 0x1e3ce508, v72
	v_max_f32_e32 v107, 0x1e3ce508, v74
	v_max_f32_e32 v106, 0x1e3ce508, v70
	v_max_f32_e32 v136, 0x1e3ce508, v2
	v_max_f32_e32 v134, 0x1e3ce508, v73
	v_max_f32_e32 v108, 0x1e3ce508, v75
	v_max_f32_e32 v2, 0x1e3ce508, v71
	s_cbranch_vccnz .LBB0_1689
	v_lshl_add_u64 v[70:71], s[8:9], 0, v[104:105]
	v_mov_b32_e32 v70, v186
	v_mov_b32_e32 v71, v187
	v_rcp_f32_e32 v1, v135
	v_rcp_f32_e32 v72, v136
	v_rcp_f32_e32 v73, v109
	v_rcp_f32_e32 v74, v134
	v_rcp_f32_e32 v75, v107
	v_rcp_f32_e32 v76, v108
	v_rcp_f32_e32 v77, v106
	v_rcp_f32_e32 v137, v2
	s_mov_b64 s[46:47], 0
	v_cvt_f32_ubyte0_e32 v138, v70
	v_cvt_f32_ubyte0_e32 v139, v71
	v_cvt_f32_ubyte1_e32 v140, v70
	v_cvt_f32_ubyte1_e32 v141, v71
	v_cvt_f32_ubyte2_e32 v158, v70
	v_cvt_f32_ubyte2_e32 v159, v71
	v_cvt_f32_ubyte3_e32 v70, v70
	v_cvt_f32_ubyte3_e32 v71, v71
	v_mul_f32_e32 v138, 0x3b808081, v138
	v_mul_f32_e32 v139, 0x3b808081, v139
	v_mul_f32_e32 v140, 0x3b808081, v140
	v_mul_f32_e32 v141, 0x3b808081, v141
	v_mul_f32_e32 v158, 0x3b808081, v158
	v_mul_f32_e32 v159, 0x3b808081, v159
	v_mul_f32_e32 v70, 0x3b808081, v70
	v_mul_f32_e32 v71, 0x3b808081, v71
	v_mul_f32_e32 v1, v1, v138
	v_mul_f32_e32 v72, v72, v139
	v_mul_f32_e32 v73, v73, v140
	v_mul_f32_e32 v138, v74, v141
	v_mul_f32_e32 v139, v75, v158
	v_mul_f32_e32 v76, v76, v159
	v_mul_f32_e32 v77, v77, v70
	v_mul_f32_e32 v137, v137, v71
	v_mul_f32_e32 v70, v90, v1
	v_mul_f32_e32 v74, v86, v72
	v_mul_f32_e32 v71, v91, v73
	v_mul_f32_e32 v75, v87, v138
	v_mul_f32_e32 v72, v92, v139
	v_mul_f32_e32 v76, v88, v76
	v_mul_f32_e32 v73, v93, v77
	v_mul_f32_e32 v77, v89, v137

.LBB0_1691:
	v_lshl_add_u64 v[102:103], v[102:103], 0, s[44:45]
	v_lshl_add_u64 v[86:87], s[10:11], 0, v[102:103]
	v_mov_b32_e32 v86, v184
	v_mov_b32_e32 v87, v185
	s_and_b64 vcc, exec, s[0:1]
	s_mov_b64 s[46:47], -1
	v_cvt_f32_ubyte0_e32 v1, v86
	v_cvt_f32_ubyte0_e32 v2, v87
	v_cvt_f32_ubyte1_e32 v88, v86
	v_cvt_f32_ubyte1_e32 v89, v87
	v_cvt_f32_ubyte2_e32 v90, v86
	v_cvt_f32_ubyte2_e32 v91, v87
	v_cvt_f32_ubyte3_e32 v86, v86
	v_cvt_f32_ubyte3_e32 v87, v87
	v_mul_f32_e32 v1, 0x3b808081, v1
	v_mul_f32_e32 v2, 0x3b808081, v2
	v_mul_f32_e32 v88, 0x3b808081, v88
	v_mul_f32_e32 v89, 0x3b808081, v89
	v_mul_f32_e32 v90, 0x3b808081, v90
	v_mul_f32_e32 v91, 0x3b808081, v91
	v_mul_f32_e32 v86, 0x3b808081, v86
	v_mul_f32_e32 v87, 0x3b808081, v87
	v_max_f32_e32 v109, 0x1e3ce508, v1
	v_max_f32_e32 v107, 0x1e3ce508, v88
	v_max_f32_e32 v105, 0x1e3ce508, v90
	v_max_f32_e32 v104, 0x1e3ce508, v86
	v_max_f32_e32 v134, 0x1e3ce508, v2
	v_max_f32_e32 v108, 0x1e3ce508, v89
	v_max_f32_e32 v106, 0x1e3ce508, v91
	v_max_f32_e32 v2, 0x1e3ce508, v87
	s_cbranch_vccnz .LBB0_1693
	v_lshl_add_u64 v[86:87], s[8:9], 0, v[102:103]
	v_mov_b32_e32 v86, v188
	v_mov_b32_e32 v87, v189
	v_rcp_f32_e32 v1, v109
	v_rcp_f32_e32 v88, v134
	v_rcp_f32_e32 v89, v107
	v_rcp_f32_e32 v90, v108
	v_rcp_f32_e32 v91, v105
	v_rcp_f32_e32 v92, v106
	v_rcp_f32_e32 v93, v104
	v_rcp_f32_e32 v135, v2
	s_mov_b64 s[46:47], 0
	v_cvt_f32_ubyte0_e32 v136, v86
	v_cvt_f32_ubyte0_e32 v137, v87
	v_cvt_f32_ubyte1_e32 v138, v86
	v_cvt_f32_ubyte1_e32 v139, v87
	v_cvt_f32_ubyte2_e32 v140, v86
	v_cvt_f32_ubyte2_e32 v141, v87
	v_cvt_f32_ubyte3_e32 v86, v86
	v_cvt_f32_ubyte3_e32 v87, v87
	v_mul_f32_e32 v136, 0x3b808081, v136
	v_mul_f32_e32 v137, 0x3b808081, v137
	v_mul_f32_e32 v138, 0x3b808081, v138
	v_mul_f32_e32 v139, 0x3b808081, v139
	v_mul_f32_e32 v140, 0x3b808081, v140
	v_mul_f32_e32 v141, 0x3b808081, v141
	v_mul_f32_e32 v86, 0x3b808081, v86
	v_mul_f32_e32 v87, 0x3b808081, v87
	v_mul_f32_e32 v1, v1, v136
	v_mul_f32_e32 v88, v88, v137
	v_mul_f32_e32 v89, v89, v138
	v_mul_f32_e32 v136, v90, v139
	v_mul_f32_e32 v137, v91, v140
	v_mul_f32_e32 v92, v92, v141
	v_mul_f32_e32 v93, v93, v86
	v_mul_f32_e32 v135, v135, v87
	v_mul_f32_e32 v86, v154, v1
	v_mul_f32_e32 v90, v150, v88
	v_mul_f32_e32 v87, v155, v89
	v_mul_f32_e32 v91, v151, v136
	v_mul_f32_e32 v88, v156, v137
	v_mul_f32_e32 v92, v152, v92
	v_mul_f32_e32 v89, v157, v93
	v_mul_f32_e32 v93, v153, v135

.LBB0_1695:
	v_lshl_add_u64 v[134:135], v[4:5], 0, s[20:21]
	v_lshl_add_u64 v[136:137], v[134:135], 0, s[42:43]
	v_lshl_add_u64 v[102:103], s[10:11], 0, v[136:137]
	v_mov_b32_e32 v102, v190
	v_mov_b32_e32 v103, v191
	s_and_b64 vcc, exec, s[0:1]
	s_mov_b64 s[46:47], -1
	v_cvt_f32_ubyte0_e32 v1, v102
	v_cvt_f32_ubyte0_e32 v2, v103
	v_cvt_f32_ubyte1_e32 v104, v102
	v_cvt_f32_ubyte1_e32 v105, v103
	v_cvt_f32_ubyte2_e32 v106, v102
	v_cvt_f32_ubyte2_e32 v107, v103
	v_cvt_f32_ubyte3_e32 v102, v102
	v_cvt_f32_ubyte3_e32 v103, v103
	v_mul_f32_e32 v1, 0x3b808081, v1
	v_mul_f32_e32 v2, 0x3b808081, v2
	v_mul_f32_e32 v104, 0x3b808081, v104
	v_mul_f32_e32 v105, 0x3b808081, v105
	v_mul_f32_e32 v106, 0x3b808081, v106
	v_mul_f32_e32 v107, 0x3b808081, v107
	v_mul_f32_e32 v102, 0x3b808081, v102
	v_mul_f32_e32 v103, 0x3b808081, v103
	v_max_f32_e32 v151, 0x1e3ce508, v1
	v_max_f32_e32 v141, 0x1e3ce508, v104
	v_max_f32_e32 v139, 0x1e3ce508, v106
	v_max_f32_e32 v138, 0x1e3ce508, v102
	v_max_f32_e32 v152, 0x1e3ce508, v2
	v_max_f32_e32 v150, 0x1e3ce508, v105
	v_max_f32_e32 v140, 0x1e3ce508, v107
	v_max_f32_e32 v2, 0x1e3ce508, v103
	s_cbranch_vccnz .LBB0_1697
	v_lshl_add_u64 v[102:103], s[8:9], 0, v[136:137]
	v_mov_b32_e32 v102, v194
	v_mov_b32_e32 v103, v195
	v_rcp_f32_e32 v1, v151
	v_rcp_f32_e32 v104, v152
	v_rcp_f32_e32 v105, v141
	v_rcp_f32_e32 v106, v150
	v_rcp_f32_e32 v107, v139
	v_rcp_f32_e32 v108, v140
	v_rcp_f32_e32 v109, v138
	v_rcp_f32_e32 v153, v2
	s_mov_b64 s[46:47], 0
	v_cvt_f32_ubyte0_e32 v154, v102
	v_cvt_f32_ubyte0_e32 v155, v103
	v_cvt_f32_ubyte1_e32 v156, v102
	v_cvt_f32_ubyte1_e32 v157, v103
	v_cvt_f32_ubyte2_e32 v158, v102
	v_cvt_f32_ubyte2_e32 v159, v103
	v_cvt_f32_ubyte3_e32 v102, v102
	v_cvt_f32_ubyte3_e32 v103, v103
	v_mul_f32_e32 v154, 0x3b808081, v154
	v_mul_f32_e32 v155, 0x3b808081, v155
	v_mul_f32_e32 v156, 0x3b808081, v156
	v_mul_f32_e32 v157, 0x3b808081, v157
	v_mul_f32_e32 v158, 0x3b808081, v158
	v_mul_f32_e32 v159, 0x3b808081, v159
	v_mul_f32_e32 v102, 0x3b808081, v102
	v_mul_f32_e32 v103, 0x3b808081, v103
	v_mul_f32_e32 v1, v1, v154
	v_mul_f32_e32 v104, v104, v155
	v_mul_f32_e32 v105, v105, v156
	v_mul_f32_e32 v154, v106, v157
	v_mul_f32_e32 v155, v107, v158
	v_mul_f32_e32 v108, v108, v159
	v_mul_f32_e32 v109, v109, v102
	v_mul_f32_e32 v153, v153, v103
	v_mul_f32_e32 v102, v122, v1
	v_mul_f32_e32 v106, v118, v104
	v_mul_f32_e32 v103, v123, v105
	v_mul_f32_e32 v107, v119, v154
	v_mul_f32_e32 v104, v124, v155
	v_mul_f32_e32 v108, v120, v108
	v_mul_f32_e32 v105, v125, v109
	v_mul_f32_e32 v109, v121, v153

.LBB0_1699:
	v_lshl_add_u64 v[134:135], v[134:135], 0, s[44:45]
	v_lshl_add_u64 v[118:119], s[10:11], 0, v[134:135]
	v_mov_b32_e32 v118, v192
	v_mov_b32_e32 v119, v193
	s_and_b64 vcc, exec, s[0:1]
	s_mov_b64 s[46:47], -1
	v_cvt_f32_ubyte0_e32 v1, v118
	v_cvt_f32_ubyte0_e32 v2, v119
	v_cvt_f32_ubyte1_e32 v120, v118
	v_cvt_f32_ubyte1_e32 v121, v119
	v_cvt_f32_ubyte2_e32 v122, v118
	v_cvt_f32_ubyte2_e32 v123, v119
	v_cvt_f32_ubyte3_e32 v118, v118
	v_cvt_f32_ubyte3_e32 v119, v119
	v_mul_f32_e32 v1, 0x3b808081, v1
	v_mul_f32_e32 v2, 0x3b808081, v2
	v_mul_f32_e32 v120, 0x3b808081, v120
	v_mul_f32_e32 v121, 0x3b808081, v121
	v_mul_f32_e32 v122, 0x3b808081, v122
	v_mul_f32_e32 v123, 0x3b808081, v123
	v_mul_f32_e32 v118, 0x3b808081, v118
	v_mul_f32_e32 v119, 0x3b808081, v119
	v_max_f32_e32 v141, 0x1e3ce508, v1
	v_max_f32_e32 v139, 0x1e3ce508, v120
	v_max_f32_e32 v137, 0x1e3ce508, v122
	v_max_f32_e32 v136, 0x1e3ce508, v118
	v_max_f32_e32 v150, 0x1e3ce508, v2
	v_max_f32_e32 v140, 0x1e3ce508, v121
	v_max_f32_e32 v138, 0x1e3ce508, v123
	v_max_f32_e32 v2, 0x1e3ce508, v119
	s_cbranch_vccnz .LBB0_1701
	v_lshl_add_u64 v[118:119], s[8:9], 0, v[134:135]
	v_mov_b32_e32 v118, v196
	v_mov_b32_e32 v119, v197
	v_rcp_f32_e32 v1, v141
	v_rcp_f32_e32 v120, v150
	v_rcp_f32_e32 v121, v139
	v_rcp_f32_e32 v122, v140
	v_rcp_f32_e32 v123, v137
	v_rcp_f32_e32 v124, v138
	v_rcp_f32_e32 v125, v136
	v_rcp_f32_e32 v151, v2
	s_mov_b64 s[46:47], 0
	v_cvt_f32_ubyte0_e32 v152, v118
	v_cvt_f32_ubyte0_e32 v153, v119
	v_cvt_f32_ubyte1_e32 v154, v118
	v_cvt_f32_ubyte1_e32 v155, v119
	v_cvt_f32_ubyte2_e32 v156, v118
	v_cvt_f32_ubyte2_e32 v157, v119
	v_cvt_f32_ubyte3_e32 v118, v118
	v_cvt_f32_ubyte3_e32 v119, v119
	v_mul_f32_e32 v152, 0x3b808081, v152
	v_mul_f32_e32 v153, 0x3b808081, v153
	v_mul_f32_e32 v154, 0x3b808081, v154
	v_mul_f32_e32 v155, 0x3b808081, v155
	v_mul_f32_e32 v156, 0x3b808081, v156
	v_mul_f32_e32 v157, 0x3b808081, v157
	v_mul_f32_e32 v118, 0x3b808081, v118
	v_mul_f32_e32 v119, 0x3b808081, v119
	v_mul_f32_e32 v1, v1, v152
	v_mul_f32_e32 v120, v120, v153
	v_mul_f32_e32 v121, v121, v154
	v_mul_f32_e32 v152, v122, v155
	v_mul_f32_e32 v153, v123, v156
	v_mul_f32_e32 v124, v124, v157
	v_mul_f32_e32 v125, v125, v118
	v_mul_f32_e32 v151, v151, v119
	v_mul_f32_e32 v118, v146, v1
	v_mul_f32_e32 v122, v142, v120
	v_mul_f32_e32 v119, v147, v121
	v_mul_f32_e32 v123, v143, v152
	v_mul_f32_e32 v120, v148, v153
	v_mul_f32_e32 v124, v144, v124
	v_mul_f32_e32 v121, v149, v125
	v_mul_f32_e32 v125, v145, v151

.LBB0_1703:
	v_lshl_add_u64 v[142:143], v[4:5], 0, s[22:23]
	v_lshl_add_u64 v[144:145], v[142:143], 0, s[42:43]
	v_lshl_add_u64 v[134:135], s[10:11], 0, v[144:145]
	v_mov_b32_e32 v134, v198
	v_mov_b32_e32 v135, v199
	s_and_b64 vcc, exec, s[0:1]
	s_mov_b64 s[46:47], -1
	v_cvt_f32_ubyte0_e32 v1, v134
	v_cvt_f32_ubyte0_e32 v2, v135
	v_cvt_f32_ubyte1_e32 v136, v134
	v_cvt_f32_ubyte1_e32 v137, v135
	v_cvt_f32_ubyte2_e32 v138, v134
	v_cvt_f32_ubyte2_e32 v139, v135
	v_cvt_f32_ubyte3_e32 v134, v134
	v_cvt_f32_ubyte3_e32 v135, v135
	v_mul_f32_e32 v1, 0x3b808081, v1
	v_mul_f32_e32 v2, 0x3b808081, v2
	v_mul_f32_e32 v136, 0x3b808081, v136
	v_mul_f32_e32 v137, 0x3b808081, v137
	v_mul_f32_e32 v138, 0x3b808081, v138
	v_mul_f32_e32 v139, 0x3b808081, v139
	v_mul_f32_e32 v134, 0x3b808081, v134
	v_mul_f32_e32 v135, 0x3b808081, v135
	v_max_f32_e32 v151, 0x1e3ce508, v1
	v_max_f32_e32 v149, 0x1e3ce508, v136
	v_max_f32_e32 v147, 0x1e3ce508, v138
	v_max_f32_e32 v146, 0x1e3ce508, v134
	v_max_f32_e32 v152, 0x1e3ce508, v2
	v_max_f32_e32 v150, 0x1e3ce508, v137
	v_max_f32_e32 v148, 0x1e3ce508, v139
	v_max_f32_e32 v2, 0x1e3ce508, v135
	s_cbranch_vccnz .LBB0_1705
	v_lshl_add_u64 v[134:135], s[8:9], 0, v[144:145]
	v_mov_b32_e32 v134, v202
	v_mov_b32_e32 v135, v203
	v_rcp_f32_e32 v1, v151
	v_rcp_f32_e32 v136, v152
	v_rcp_f32_e32 v137, v149
	v_rcp_f32_e32 v138, v150
	v_rcp_f32_e32 v139, v147
	v_rcp_f32_e32 v140, v148
	v_rcp_f32_e32 v141, v146
	v_rcp_f32_e32 v153, v2
	s_mov_b64 s[46:47], 0
	v_cvt_f32_ubyte0_e32 v154, v134
	v_cvt_f32_ubyte0_e32 v155, v135
	v_cvt_f32_ubyte1_e32 v156, v134
	v_cvt_f32_ubyte1_e32 v157, v135
	v_cvt_f32_ubyte2_e32 v158, v134
	v_cvt_f32_ubyte2_e32 v159, v135
	v_cvt_f32_ubyte3_e32 v134, v134
	v_cvt_f32_ubyte3_e32 v135, v135
	v_mul_f32_e32 v154, 0x3b808081, v154
	v_mul_f32_e32 v155, 0x3b808081, v155
	v_mul_f32_e32 v156, 0x3b808081, v156
	v_mul_f32_e32 v157, 0x3b808081, v157
	v_mul_f32_e32 v158, 0x3b808081, v158
	v_mul_f32_e32 v159, 0x3b808081, v159
	v_mul_f32_e32 v134, 0x3b808081, v134
	v_mul_f32_e32 v135, 0x3b808081, v135
	v_mul_f32_e32 v1, v1, v154
	v_mul_f32_e32 v136, v136, v155
	v_mul_f32_e32 v137, v137, v156
	v_mul_f32_e32 v154, v138, v157
	v_mul_f32_e32 v155, v139, v158
	v_mul_f32_e32 v140, v140, v159
	v_mul_f32_e32 v141, v141, v134
	v_mul_f32_e32 v153, v153, v135
	v_mul_f32_e32 v134, v130, v1
	v_mul_f32_e32 v138, v126, v136
	v_mul_f32_e32 v135, v131, v137
	v_mul_f32_e32 v139, v127, v154
	v_mul_f32_e32 v136, v132, v155
	v_mul_f32_e32 v140, v128, v140
	v_mul_f32_e32 v137, v133, v141
	v_mul_f32_e32 v141, v129, v153

.LBB0_1707:
	v_lshl_add_u64 v[142:143], v[142:143], 0, s[44:45]
	v_lshl_add_u64 v[126:127], s[10:11], 0, v[142:143]
	v_mov_b32_e32 v126, v200
	v_mov_b32_e32 v127, v201
	s_and_b64 vcc, exec, s[0:1]
	s_mov_b64 s[46:47], -1
	v_cvt_f32_ubyte0_e32 v1, v126
	v_cvt_f32_ubyte0_e32 v2, v127
	v_cvt_f32_ubyte1_e32 v128, v126
	v_cvt_f32_ubyte1_e32 v129, v127
	v_cvt_f32_ubyte2_e32 v130, v126
	v_cvt_f32_ubyte2_e32 v131, v127
	v_cvt_f32_ubyte3_e32 v126, v126
	v_cvt_f32_ubyte3_e32 v127, v127
	v_mul_f32_e32 v1, 0x3b808081, v1
	v_mul_f32_e32 v2, 0x3b808081, v2
	v_mul_f32_e32 v128, 0x3b808081, v128
	v_mul_f32_e32 v129, 0x3b808081, v129
	v_mul_f32_e32 v130, 0x3b808081, v130
	v_mul_f32_e32 v131, 0x3b808081, v131
	v_mul_f32_e32 v126, 0x3b808081, v126
	v_mul_f32_e32 v127, 0x3b808081, v127
	v_max_f32_e32 v149, 0x1e3ce508, v1
	v_max_f32_e32 v147, 0x1e3ce508, v128
	v_max_f32_e32 v145, 0x1e3ce508, v130
	v_max_f32_e32 v144, 0x1e3ce508, v126
	v_max_f32_e32 v150, 0x1e3ce508, v2
	v_max_f32_e32 v148, 0x1e3ce508, v129
	v_max_f32_e32 v146, 0x1e3ce508, v131
	v_max_f32_e32 v2, 0x1e3ce508, v127
	s_cbranch_vccnz .LBB0_1709
	v_lshl_add_u64 v[126:127], s[8:9], 0, v[142:143]
	v_mov_b32_e32 v126, v204
	v_mov_b32_e32 v127, v205
	v_rcp_f32_e32 v1, v149
	v_rcp_f32_e32 v128, v150
	v_rcp_f32_e32 v129, v147
	v_rcp_f32_e32 v130, v148
	v_rcp_f32_e32 v131, v145
	v_rcp_f32_e32 v132, v146
	v_rcp_f32_e32 v133, v144
	v_rcp_f32_e32 v151, v2
	s_mov_b64 s[46:47], 0
	v_cvt_f32_ubyte0_e32 v152, v126
	v_cvt_f32_ubyte0_e32 v153, v127
	v_cvt_f32_ubyte1_e32 v154, v126
	v_cvt_f32_ubyte1_e32 v155, v127
	v_cvt_f32_ubyte2_e32 v156, v126
	v_cvt_f32_ubyte2_e32 v157, v127
	v_cvt_f32_ubyte3_e32 v126, v126
	v_cvt_f32_ubyte3_e32 v127, v127
	v_mul_f32_e32 v152, 0x3b808081, v152
	v_mul_f32_e32 v153, 0x3b808081, v153
	v_mul_f32_e32 v154, 0x3b808081, v154
	v_mul_f32_e32 v155, 0x3b808081, v155
	v_mul_f32_e32 v156, 0x3b808081, v156
	v_mul_f32_e32 v157, 0x3b808081, v157
	v_mul_f32_e32 v126, 0x3b808081, v126
	v_mul_f32_e32 v127, 0x3b808081, v127
	v_mul_f32_e32 v1, v1, v152
	v_mul_f32_e32 v128, v128, v153
	v_mul_f32_e32 v129, v129, v154
	v_mul_f32_e32 v152, v130, v155
	v_mul_f32_e32 v153, v131, v156
	v_mul_f32_e32 v132, v132, v157
	v_mul_f32_e32 v133, v133, v126
	v_mul_f32_e32 v151, v151, v127
	v_mul_f32_e32 v126, v114, v1
	v_mul_f32_e32 v130, v110, v128
	v_mul_f32_e32 v127, v115, v129
	v_mul_f32_e32 v131, v111, v152
	v_mul_f32_e32 v128, v116, v153
	v_mul_f32_e32 v132, v112, v132
	v_mul_f32_e32 v129, v117, v133
	v_mul_f32_e32 v133, v113, v151

.LBB0_1711:
	s_mov_b64 s[46:47], 0x40000
	v_lshl_add_u64 v[142:143], v[4:5], 0, s[46:47]
	v_lshl_add_u64 v[144:145], v[142:143], 0, s[42:43]
	v_lshl_add_u64 v[110:111], s[10:11], 0, v[144:145]
	v_mov_b32_e32 v110, v206
	v_mov_b32_e32 v111, v207
	s_and_b64 vcc, exec, s[0:1]
	s_mov_b64 s[46:47], -1
	v_cvt_f32_ubyte0_e32 v1, v110
	v_cvt_f32_ubyte0_e32 v2, v111
	v_cvt_f32_ubyte1_e32 v112, v110
	v_cvt_f32_ubyte1_e32 v113, v111
	v_cvt_f32_ubyte2_e32 v114, v110
	v_cvt_f32_ubyte2_e32 v115, v111
	v_cvt_f32_ubyte3_e32 v110, v110
	v_cvt_f32_ubyte3_e32 v111, v111
	v_mul_f32_e32 v1, 0x3b808081, v1
	v_mul_f32_e32 v2, 0x3b808081, v2
	v_mul_f32_e32 v112, 0x3b808081, v112
	v_mul_f32_e32 v113, 0x3b808081, v113
	v_mul_f32_e32 v114, 0x3b808081, v114
	v_mul_f32_e32 v115, 0x3b808081, v115
	v_mul_f32_e32 v110, 0x3b808081, v110
	v_mul_f32_e32 v111, 0x3b808081, v111
	v_max_f32_e32 v151, 0x1e3ce508, v1
	v_max_f32_e32 v149, 0x1e3ce508, v112
	v_max_f32_e32 v147, 0x1e3ce508, v114
	v_max_f32_e32 v146, 0x1e3ce508, v110
	v_max_f32_e32 v152, 0x1e3ce508, v2
	v_max_f32_e32 v150, 0x1e3ce508, v113
	v_max_f32_e32 v148, 0x1e3ce508, v115
	v_max_f32_e32 v2, 0x1e3ce508, v111
	s_cbranch_vccnz .LBB0_1713
	v_lshl_add_u64 v[110:111], s[8:9], 0, v[144:145]
	v_mov_b32_e32 v110, v210
	v_mov_b32_e32 v111, v211
	v_rcp_f32_e32 v1, v151
	v_rcp_f32_e32 v112, v152
	v_rcp_f32_e32 v113, v149
	v_rcp_f32_e32 v114, v150
	v_rcp_f32_e32 v115, v147
	v_rcp_f32_e32 v116, v148
	v_rcp_f32_e32 v117, v146
	v_rcp_f32_e32 v153, v2
	s_mov_b64 s[46:47], 0
	v_cvt_f32_ubyte0_e32 v154, v110
	v_cvt_f32_ubyte0_e32 v155, v111
	v_cvt_f32_ubyte1_e32 v156, v110
	v_cvt_f32_ubyte1_e32 v157, v111
	v_cvt_f32_ubyte2_e32 v158, v110
	v_cvt_f32_ubyte2_e32 v159, v111
	v_cvt_f32_ubyte3_e32 v110, v110
	v_cvt_f32_ubyte3_e32 v111, v111
	v_mul_f32_e32 v154, 0x3b808081, v154
	v_mul_f32_e32 v155, 0x3b808081, v155
	v_mul_f32_e32 v156, 0x3b808081, v156
	v_mul_f32_e32 v157, 0x3b808081, v157
	v_mul_f32_e32 v158, 0x3b808081, v158
	v_mul_f32_e32 v159, 0x3b808081, v159
	v_mul_f32_e32 v110, 0x3b808081, v110
	v_mul_f32_e32 v111, 0x3b808081, v111
	v_mul_f32_e32 v1, v1, v154
	v_mul_f32_e32 v112, v112, v155
	v_mul_f32_e32 v113, v113, v156
	v_mul_f32_e32 v154, v114, v157
	v_mul_f32_e32 v155, v115, v158
	v_mul_f32_e32 v116, v116, v159
	v_mul_f32_e32 v117, v117, v110
	v_mul_f32_e32 v153, v153, v111
	v_mul_f32_e32 v110, v98, v1
	v_mul_f32_e32 v114, v94, v112
	v_mul_f32_e32 v111, v99, v113
	v_mul_f32_e32 v115, v95, v154
	v_mul_f32_e32 v112, v100, v155
	v_mul_f32_e32 v116, v96, v116
	v_mul_f32_e32 v113, v101, v117
	v_mul_f32_e32 v117, v97, v153

.LBB0_1715:
	v_lshl_add_u64 v[142:143], v[142:143], 0, s[44:45]
	v_lshl_add_u64 v[94:95], s[10:11], 0, v[142:143]
	v_mov_b32_e32 v94, v208
	v_mov_b32_e32 v95, v209
	s_and_b64 vcc, exec, s[0:1]
	s_mov_b64 s[46:47], -1
	v_cvt_f32_ubyte0_e32 v1, v94
	v_cvt_f32_ubyte0_e32 v2, v95
	v_cvt_f32_ubyte1_e32 v96, v94
	v_cvt_f32_ubyte1_e32 v97, v95
	v_cvt_f32_ubyte2_e32 v98, v94
	v_cvt_f32_ubyte2_e32 v99, v95
	v_cvt_f32_ubyte3_e32 v94, v94
	v_cvt_f32_ubyte3_e32 v95, v95
	v_mul_f32_e32 v1, 0x3b808081, v1
	v_mul_f32_e32 v2, 0x3b808081, v2
	v_mul_f32_e32 v96, 0x3b808081, v96
	v_mul_f32_e32 v97, 0x3b808081, v97
	v_mul_f32_e32 v98, 0x3b808081, v98
	v_mul_f32_e32 v99, 0x3b808081, v99
	v_mul_f32_e32 v94, 0x3b808081, v94
	v_mul_f32_e32 v95, 0x3b808081, v95
	v_max_f32_e32 v149, 0x1e3ce508, v1
	v_max_f32_e32 v147, 0x1e3ce508, v96
	v_max_f32_e32 v145, 0x1e3ce508, v98
	v_max_f32_e32 v144, 0x1e3ce508, v94
	v_max_f32_e32 v150, 0x1e3ce508, v2
	v_max_f32_e32 v148, 0x1e3ce508, v97
	v_max_f32_e32 v146, 0x1e3ce508, v99
	v_max_f32_e32 v2, 0x1e3ce508, v95
	s_cbranch_vccnz .LBB0_1717
	v_lshl_add_u64 v[94:95], s[8:9], 0, v[142:143]
	v_mov_b32_e32 v94, v212
	v_mov_b32_e32 v95, v213
	v_rcp_f32_e32 v1, v149
	v_rcp_f32_e32 v96, v150
	v_rcp_f32_e32 v97, v147
	v_rcp_f32_e32 v98, v148
	v_rcp_f32_e32 v99, v145
	v_rcp_f32_e32 v100, v146
	v_rcp_f32_e32 v101, v144
	v_rcp_f32_e32 v151, v2
	s_mov_b64 s[46:47], 0
	v_cvt_f32_ubyte0_e32 v152, v94
	v_cvt_f32_ubyte0_e32 v153, v95
	v_cvt_f32_ubyte1_e32 v154, v94
	v_cvt_f32_ubyte1_e32 v155, v95
	v_cvt_f32_ubyte2_e32 v156, v94
	v_cvt_f32_ubyte2_e32 v157, v95
	v_cvt_f32_ubyte3_e32 v94, v94
	v_cvt_f32_ubyte3_e32 v95, v95
	v_mul_f32_e32 v152, 0x3b808081, v152
	v_mul_f32_e32 v153, 0x3b808081, v153
	v_mul_f32_e32 v154, 0x3b808081, v154
	v_mul_f32_e32 v155, 0x3b808081, v155
	v_mul_f32_e32 v156, 0x3b808081, v156
	v_mul_f32_e32 v157, 0x3b808081, v157
	v_mul_f32_e32 v94, 0x3b808081, v94
	v_mul_f32_e32 v95, 0x3b808081, v95
	v_mul_f32_e32 v1, v1, v152
	v_mul_f32_e32 v96, v96, v153
	v_mul_f32_e32 v97, v97, v154
	v_mul_f32_e32 v152, v98, v155
	v_mul_f32_e32 v153, v99, v156
	v_mul_f32_e32 v100, v100, v157
	v_mul_f32_e32 v101, v101, v94
	v_mul_f32_e32 v151, v151, v95
	v_mul_f32_e32 v94, v82, v1
	v_mul_f32_e32 v98, v78, v96
	v_mul_f32_e32 v95, v83, v97
	v_mul_f32_e32 v99, v79, v152
	v_mul_f32_e32 v96, v84, v153
	v_mul_f32_e32 v100, v80, v100
	v_mul_f32_e32 v97, v85, v101
	v_mul_f32_e32 v101, v81, v151

.LBB0_1719:
	v_lshl_add_u64 v[78:79], v[4:5], 0, s[24:25]
	v_lshl_add_u64 v[80:81], v[78:79], 0, s[42:43]
	v_lshl_add_u64 v[82:83], s[10:11], 0, v[80:81]
	v_mov_b32_e32 v82, v214
	v_mov_b32_e32 v83, v215
	s_and_b64 vcc, exec, s[0:1]
	s_mov_b64 s[46:47], -1
	v_cvt_f32_ubyte0_e32 v1, v82
	v_cvt_f32_ubyte0_e32 v2, v83
	v_cvt_f32_ubyte1_e32 v84, v82
	v_cvt_f32_ubyte1_e32 v85, v83
	v_cvt_f32_ubyte2_e32 v142, v82
	v_cvt_f32_ubyte2_e32 v143, v83
	v_cvt_f32_ubyte3_e32 v82, v82
	v_cvt_f32_ubyte3_e32 v83, v83
	v_mul_f32_e32 v1, 0x3b808081, v1
	v_mul_f32_e32 v2, 0x3b808081, v2
	v_mul_f32_e32 v84, 0x3b808081, v84
	v_mul_f32_e32 v144, 0x3b808081, v85
	v_mul_f32_e32 v142, 0x3b808081, v142
	v_mul_f32_e32 v143, 0x3b808081, v143
	v_mul_f32_e32 v82, 0x3b808081, v82
	v_mul_f32_e32 v145, 0x3b808081, v83
	v_max_f32_e32 v151, 0x1e3ce508, v1
	v_max_f32_e32 v85, 0x1e3ce508, v84
	v_max_f32_e32 v83, 0x1e3ce508, v142
	v_max_f32_e32 v82, 0x1e3ce508, v82
	v_max_f32_e32 v152, 0x1e3ce508, v2
	v_max_f32_e32 v150, 0x1e3ce508, v144
	v_max_f32_e32 v84, 0x1e3ce508, v143
	v_max_f32_e32 v2, 0x1e3ce508, v145
	s_cbranch_vccnz .LBB0_1721
	v_lshl_add_u64 v[142:143], s[8:9], 0, v[80:81]
	v_mov_b32_e32 v142, v218
	v_mov_b32_e32 v143, v219
	v_rcp_f32_e32 v1, v151
	v_rcp_f32_e32 v144, v152
	v_rcp_f32_e32 v145, v85
	v_rcp_f32_e32 v146, v150
	v_rcp_f32_e32 v147, v83
	v_rcp_f32_e32 v148, v84
	v_rcp_f32_e32 v149, v82
	v_rcp_f32_e32 v153, v2
	s_mov_b64 s[46:47], 0
	v_cvt_f32_ubyte0_e32 v154, v142
	v_cvt_f32_ubyte0_e32 v155, v143
	v_cvt_f32_ubyte1_e32 v156, v142
	v_cvt_f32_ubyte1_e32 v157, v143
	v_cvt_f32_ubyte2_e32 v158, v142
	v_cvt_f32_ubyte2_e32 v159, v143
	v_cvt_f32_ubyte3_e32 v142, v142
	v_cvt_f32_ubyte3_e32 v143, v143
	v_mul_f32_e32 v154, 0x3b808081, v154
	v_mul_f32_e32 v155, 0x3b808081, v155
	v_mul_f32_e32 v156, 0x3b808081, v156
	v_mul_f32_e32 v157, 0x3b808081, v157
	v_mul_f32_e32 v158, 0x3b808081, v158
	v_mul_f32_e32 v159, 0x3b808081, v159
	v_mul_f32_e32 v142, 0x3b808081, v142
	v_mul_f32_e32 v143, 0x3b808081, v143
	v_mul_f32_e32 v1, v1, v154
	v_mul_f32_e32 v144, v144, v155
	v_mul_f32_e32 v145, v145, v156
	v_mul_f32_e32 v154, v146, v157
	v_mul_f32_e32 v155, v147, v158
	v_mul_f32_e32 v148, v148, v159
	v_mul_f32_e32 v149, v149, v142
	v_mul_f32_e32 v153, v153, v143
	v_mul_f32_e32 v142, v66, v1
	v_mul_f32_e32 v146, v62, v144
	v_mul_f32_e32 v143, v67, v145
	v_mul_f32_e32 v147, v63, v154
	v_mul_f32_e32 v144, v68, v155
	v_mul_f32_e32 v148, v64, v148
	v_mul_f32_e32 v145, v69, v149
	v_mul_f32_e32 v149, v65, v153

.LBB0_1723:
	v_lshl_add_u64 v[78:79], v[78:79], 0, s[44:45]
	v_lshl_add_u64 v[62:63], s[10:11], 0, v[78:79]
	v_mov_b32_e32 v62, v216
	v_mov_b32_e32 v63, v217
	s_and_b64 vcc, exec, s[0:1]
	s_mov_b64 s[46:47], -1
	v_cvt_f32_ubyte0_e32 v1, v62
	v_cvt_f32_ubyte0_e32 v2, v63
	v_cvt_f32_ubyte1_e32 v64, v62
	v_cvt_f32_ubyte1_e32 v65, v63
	v_cvt_f32_ubyte2_e32 v66, v62
	v_cvt_f32_ubyte2_e32 v67, v63
	v_cvt_f32_ubyte3_e32 v62, v62
	v_cvt_f32_ubyte3_e32 v63, v63
	v_mul_f32_e32 v1, 0x3b808081, v1
	v_mul_f32_e32 v2, 0x3b808081, v2
	v_mul_f32_e32 v64, 0x3b808081, v64
	v_mul_f32_e32 v65, 0x3b808081, v65
	v_mul_f32_e32 v66, 0x3b808081, v66
	v_mul_f32_e32 v67, 0x3b808081, v67
	v_mul_f32_e32 v62, 0x3b808081, v62
	v_mul_f32_e32 v63, 0x3b808081, v63
	v_max_f32_e32 v85, 0x1e3ce508, v1
	v_max_f32_e32 v83, 0x1e3ce508, v64
	v_max_f32_e32 v81, 0x1e3ce508, v66
	v_max_f32_e32 v80, 0x1e3ce508, v62
	v_max_f32_e32 v150, 0x1e3ce508, v2
	v_max_f32_e32 v84, 0x1e3ce508, v65
	v_max_f32_e32 v82, 0x1e3ce508, v67
	v_max_f32_e32 v2, 0x1e3ce508, v63
	s_cbranch_vccnz .LBB0_1725
	v_lshl_add_u64 v[62:63], s[8:9], 0, v[78:79]
	v_mov_b32_e32 v62, v220
	v_mov_b32_e32 v63, v221
	v_rcp_f32_e32 v1, v85
	v_rcp_f32_e32 v64, v150
	v_rcp_f32_e32 v65, v83
	v_rcp_f32_e32 v66, v84
	v_rcp_f32_e32 v67, v81
	v_rcp_f32_e32 v68, v82
	v_rcp_f32_e32 v69, v80
	v_rcp_f32_e32 v151, v2
	s_mov_b64 s[46:47], 0
	v_cvt_f32_ubyte0_e32 v152, v62
	v_cvt_f32_ubyte0_e32 v153, v63
	v_cvt_f32_ubyte1_e32 v154, v62
	v_cvt_f32_ubyte1_e32 v155, v63
	v_cvt_f32_ubyte2_e32 v156, v62
	v_cvt_f32_ubyte2_e32 v157, v63
	v_cvt_f32_ubyte3_e32 v62, v62
	v_cvt_f32_ubyte3_e32 v63, v63
	v_mul_f32_e32 v152, 0x3b808081, v152
	v_mul_f32_e32 v153, 0x3b808081, v153
	v_mul_f32_e32 v154, 0x3b808081, v154
	v_mul_f32_e32 v155, 0x3b808081, v155
	v_mul_f32_e32 v156, 0x3b808081, v156
	v_mul_f32_e32 v157, 0x3b808081, v157
	v_mul_f32_e32 v62, 0x3b808081, v62
	v_mul_f32_e32 v63, 0x3b808081, v63
	v_mul_f32_e32 v1, v1, v152
	v_mul_f32_e32 v64, v64, v153
	v_mul_f32_e32 v65, v65, v154
	v_mul_f32_e32 v152, v66, v155
	v_mul_f32_e32 v153, v67, v156
	v_mul_f32_e32 v68, v68, v157
	v_mul_f32_e32 v69, v69, v62
	v_mul_f32_e32 v151, v151, v63
	v_mul_f32_e32 v62, v50, v1
	v_mul_f32_e32 v66, v46, v64
	v_mul_f32_e32 v63, v51, v65
	v_mul_f32_e32 v67, v47, v152
	v_mul_f32_e32 v64, v52, v153
	v_mul_f32_e32 v68, v48, v68
	v_mul_f32_e32 v65, v53, v69
	v_mul_f32_e32 v69, v49, v151

.LBB0_1727:
	v_lshl_add_u64 v[46:47], v[4:5], 0, s[26:27]
	v_lshl_add_u64 v[48:49], v[46:47], 0, s[42:43]
	v_lshl_add_u64 v[50:51], s[10:11], 0, v[48:49]
	v_mov_b32_e32 v50, v222
	v_mov_b32_e32 v51, v223
	s_and_b64 vcc, exec, s[0:1]
	s_mov_b64 s[46:47], -1
	v_cvt_f32_ubyte0_e32 v1, v50
	v_cvt_f32_ubyte0_e32 v2, v51
	v_cvt_f32_ubyte1_e32 v52, v50
	v_cvt_f32_ubyte1_e32 v53, v51
	v_cvt_f32_ubyte2_e32 v78, v50
	v_cvt_f32_ubyte2_e32 v79, v51
	v_cvt_f32_ubyte3_e32 v50, v50
	v_cvt_f32_ubyte3_e32 v51, v51
	v_mul_f32_e32 v1, 0x3b808081, v1
	v_mul_f32_e32 v2, 0x3b808081, v2
	v_mul_f32_e32 v52, 0x3b808081, v52
	v_mul_f32_e32 v81, 0x3b808081, v53
	v_mul_f32_e32 v78, 0x3b808081, v78
	v_mul_f32_e32 v82, 0x3b808081, v79
	v_mul_f32_e32 v50, 0x3b808081, v50
	v_mul_f32_e32 v83, 0x3b808081, v51
	v_max_f32_e32 v79, 0x1e3ce508, v1
	v_max_f32_e32 v53, 0x1e3ce508, v52
	v_max_f32_e32 v51, 0x1e3ce508, v78
	v_max_f32_e32 v50, 0x1e3ce508, v50
	v_max_f32_e32 v80, 0x1e3ce508, v2
	v_max_f32_e32 v78, 0x1e3ce508, v81
	v_max_f32_e32 v52, 0x1e3ce508, v82
	v_max_f32_e32 v2, 0x1e3ce508, v83
	s_cbranch_vccnz .LBB0_1729
	v_lshl_add_u64 v[82:83], s[8:9], 0, v[48:49]
	v_mov_b32_e32 v82, v226
	v_mov_b32_e32 v83, v227
	v_rcp_f32_e32 v1, v79
	v_rcp_f32_e32 v81, v80
	v_rcp_f32_e32 v84, v53
	v_rcp_f32_e32 v85, v78
	v_rcp_f32_e32 v150, v51
	v_rcp_f32_e32 v151, v52
	v_rcp_f32_e32 v152, v50
	v_rcp_f32_e32 v153, v2
	s_mov_b64 s[46:47], 0
	v_cvt_f32_ubyte0_e32 v154, v82
	v_cvt_f32_ubyte0_e32 v155, v83
	v_cvt_f32_ubyte1_e32 v156, v82
	v_cvt_f32_ubyte1_e32 v157, v83
	v_cvt_f32_ubyte2_e32 v158, v82
	v_cvt_f32_ubyte2_e32 v159, v83
	v_cvt_f32_ubyte3_e32 v82, v82
	v_cvt_f32_ubyte3_e32 v83, v83
	v_mul_f32_e32 v154, 0x3b808081, v154
	v_mul_f32_e32 v155, 0x3b808081, v155
	v_mul_f32_e32 v156, 0x3b808081, v156
	v_mul_f32_e32 v157, 0x3b808081, v157
	v_mul_f32_e32 v158, 0x3b808081, v158
	v_mul_f32_e32 v159, 0x3b808081, v159
	v_mul_f32_e32 v82, 0x3b808081, v82
	v_mul_f32_e32 v83, 0x3b808081, v83
	v_mul_f32_e32 v1, v1, v154
	v_mul_f32_e32 v81, v81, v155
	v_mul_f32_e32 v84, v84, v156
	v_mul_f32_e32 v85, v85, v157
	v_mul_f32_e32 v156, v150, v158
	v_mul_f32_e32 v157, v151, v159
	v_mul_f32_e32 v82, v152, v82
	v_mul_f32_e32 v83, v153, v83
	v_mul_f32_e32 v150, v34, v1
	v_mul_f32_e32 v154, v30, v81
	v_mul_f32_e32 v151, v35, v84
	v_mul_f32_e32 v155, v31, v85
	v_mul_f32_e32 v152, v36, v156
	v_mul_f32_e32 v156, v32, v157
	v_mul_f32_e32 v153, v37, v82
	v_mul_f32_e32 v157, v33, v83

.LBB0_1731:
	v_lshl_add_u64 v[46:47], v[46:47], 0, s[44:45]
	v_lshl_add_u64 v[30:31], s[10:11], 0, v[46:47]
	v_mov_b32_e32 v30, v224
	v_mov_b32_e32 v31, v225
	s_and_b64 vcc, exec, s[0:1]
	s_mov_b64 s[46:47], -1
	v_cvt_f32_ubyte0_e32 v1, v30
	v_cvt_f32_ubyte0_e32 v2, v31
	v_cvt_f32_ubyte1_e32 v32, v30
	v_cvt_f32_ubyte1_e32 v33, v31
	v_cvt_f32_ubyte2_e32 v34, v30
	v_cvt_f32_ubyte2_e32 v35, v31
	v_cvt_f32_ubyte3_e32 v30, v30
	v_cvt_f32_ubyte3_e32 v31, v31
	v_mul_f32_e32 v1, 0x3b808081, v1
	v_mul_f32_e32 v2, 0x3b808081, v2
	v_mul_f32_e32 v32, 0x3b808081, v32
	v_mul_f32_e32 v33, 0x3b808081, v33
	v_mul_f32_e32 v34, 0x3b808081, v34
	v_mul_f32_e32 v35, 0x3b808081, v35
	v_mul_f32_e32 v30, 0x3b808081, v30
	v_mul_f32_e32 v31, 0x3b808081, v31
	v_max_f32_e32 v53, 0x1e3ce508, v1
	v_max_f32_e32 v51, 0x1e3ce508, v32
	v_max_f32_e32 v49, 0x1e3ce508, v34
	v_max_f32_e32 v48, 0x1e3ce508, v30
	v_max_f32_e32 v78, 0x1e3ce508, v2
	v_max_f32_e32 v52, 0x1e3ce508, v33
	v_max_f32_e32 v50, 0x1e3ce508, v35
	v_max_f32_e32 v2, 0x1e3ce508, v31
	s_cbranch_vccnz .LBB0_1733
	v_lshl_add_u64 v[30:31], s[8:9], 0, v[46:47]
	v_mov_b32_e32 v30, v228
	v_mov_b32_e32 v31, v229
	v_rcp_f32_e32 v1, v53
	v_rcp_f32_e32 v32, v78
	v_rcp_f32_e32 v33, v51
	v_rcp_f32_e32 v34, v52
	v_rcp_f32_e32 v35, v49
	v_rcp_f32_e32 v36, v50
	v_rcp_f32_e32 v37, v48
	v_rcp_f32_e32 v79, v2
	s_mov_b64 s[46:47], 0
	v_cvt_f32_ubyte0_e32 v80, v30
	v_cvt_f32_ubyte0_e32 v81, v31
	v_cvt_f32_ubyte1_e32 v82, v30
	v_cvt_f32_ubyte1_e32 v83, v31
	v_cvt_f32_ubyte2_e32 v84, v30
	v_cvt_f32_ubyte2_e32 v85, v31
	v_cvt_f32_ubyte3_e32 v30, v30
	v_cvt_f32_ubyte3_e32 v31, v31
	v_mul_f32_e32 v80, 0x3b808081, v80
	v_mul_f32_e32 v81, 0x3b808081, v81
	v_mul_f32_e32 v82, 0x3b808081, v82
	v_mul_f32_e32 v83, 0x3b808081, v83
	v_mul_f32_e32 v84, 0x3b808081, v84
	v_mul_f32_e32 v85, 0x3b808081, v85
	v_mul_f32_e32 v30, 0x3b808081, v30
	v_mul_f32_e32 v31, 0x3b808081, v31
	v_mul_f32_e32 v1, v1, v80
	v_mul_f32_e32 v32, v32, v81
	v_mul_f32_e32 v33, v33, v82
	v_mul_f32_e32 v80, v34, v83
	v_mul_f32_e32 v81, v35, v84
	v_mul_f32_e32 v36, v36, v85
	v_mul_f32_e32 v37, v37, v30
	v_mul_f32_e32 v79, v79, v31
	v_mul_f32_e32 v30, v26, v1
	v_mul_f32_e32 v34, v22, v32
	v_mul_f32_e32 v31, v27, v33
	v_mul_f32_e32 v35, v23, v80
	v_mul_f32_e32 v32, v28, v81
	v_mul_f32_e32 v36, v24, v36
	v_mul_f32_e32 v33, v29, v37
	v_mul_f32_e32 v37, v25, v79

.LBB0_1735:
	v_lshl_add_u64 v[4:5], v[4:5], 0, s[28:29]
	v_lshl_add_u64 v[22:23], v[4:5], 0, s[42:43]
	v_lshl_add_u64 v[24:25], s[10:11], 0, v[22:23]
	v_mov_b32_e32 v24, v230
	v_mov_b32_e32 v25, v231
	s_and_b64 vcc, exec, s[0:1]
	s_mov_b64 s[42:43], -1
	v_cvt_f32_ubyte0_e32 v1, v24
	v_cvt_f32_ubyte0_e32 v2, v25
	v_cvt_f32_ubyte1_e32 v26, v24
	v_cvt_f32_ubyte1_e32 v27, v25
	v_cvt_f32_ubyte2_e32 v28, v24
	v_cvt_f32_ubyte2_e32 v29, v25
	v_cvt_f32_ubyte3_e32 v24, v24
	v_cvt_f32_ubyte3_e32 v25, v25
	v_mul_f32_e32 v1, 0x3b808081, v1
	v_mul_f32_e32 v2, 0x3b808081, v2
	v_mul_f32_e32 v26, 0x3b808081, v26
	v_mul_f32_e32 v47, 0x3b808081, v27
	v_mul_f32_e32 v28, 0x3b808081, v28
	v_mul_f32_e32 v48, 0x3b808081, v29
	v_mul_f32_e32 v24, 0x3b808081, v24
	v_mul_f32_e32 v49, 0x3b808081, v25
	v_max_f32_e32 v29, 0x1e3ce508, v1
	v_max_f32_e32 v27, 0x1e3ce508, v26
	v_max_f32_e32 v25, 0x1e3ce508, v28
	v_max_f32_e32 v24, 0x1e3ce508, v24
	v_max_f32_e32 v46, 0x1e3ce508, v2
	v_max_f32_e32 v28, 0x1e3ce508, v47
	v_max_f32_e32 v26, 0x1e3ce508, v48
	v_max_f32_e32 v2, 0x1e3ce508, v49
	s_cbranch_vccnz .LBB0_1737
	v_lshl_add_u64 v[48:49], s[8:9], 0, v[22:23]
	v_mov_b32_e32 v48, v234
	v_mov_b32_e32 v49, v235
	v_rcp_f32_e32 v1, v29
	v_rcp_f32_e32 v47, v46
	v_rcp_f32_e32 v50, v27
	v_rcp_f32_e32 v51, v28
	v_rcp_f32_e32 v52, v25
	v_rcp_f32_e32 v53, v26
	v_rcp_f32_e32 v78, v24
	v_rcp_f32_e32 v79, v2
	s_mov_b64 s[42:43], 0
	v_cvt_f32_ubyte0_e32 v80, v48
	v_cvt_f32_ubyte0_e32 v81, v49
	v_cvt_f32_ubyte1_e32 v82, v48
	v_cvt_f32_ubyte1_e32 v83, v49
	v_cvt_f32_ubyte2_e32 v84, v48
	v_cvt_f32_ubyte2_e32 v85, v49
	v_cvt_f32_ubyte3_e32 v48, v48
	v_cvt_f32_ubyte3_e32 v49, v49
	v_mul_f32_e32 v80, 0x3b808081, v80
	v_mul_f32_e32 v81, 0x3b808081, v81
	v_mul_f32_e32 v82, 0x3b808081, v82
	v_mul_f32_e32 v83, 0x3b808081, v83
	v_mul_f32_e32 v84, 0x3b808081, v84
	v_mul_f32_e32 v85, 0x3b808081, v85
	v_mul_f32_e32 v48, 0x3b808081, v48
	v_mul_f32_e32 v49, 0x3b808081, v49
	v_mul_f32_e32 v1, v1, v80
	v_mul_f32_e32 v47, v47, v81
	v_mul_f32_e32 v50, v50, v82
	v_mul_f32_e32 v51, v51, v83
	v_mul_f32_e32 v52, v52, v84
	v_mul_f32_e32 v53, v53, v85
	v_mul_f32_e32 v48, v78, v48
	v_mul_f32_e32 v49, v79, v49
	v_mul_f32_e32 v158, v18, v1
	v_mul_f32_e32 v162, v14, v47
	v_mul_f32_e32 v159, v19, v50
	v_mul_f32_e32 v163, v15, v51
	v_mul_f32_e32 v160, v20, v52
	v_mul_f32_e32 v164, v16, v53
	v_mul_f32_e32 v161, v21, v48
	v_mul_f32_e32 v165, v17, v49

.LBB0_1739:
	v_lshl_add_u64 v[4:5], v[4:5], 0, s[44:45]
	v_lshl_add_u64 v[14:15], s[10:11], 0, v[4:5]
	v_mov_b32_e32 v14, v232
	v_mov_b32_e32 v15, v233
	s_and_b64 vcc, exec, s[0:1]
	s_mov_b64 s[0:1], -1
	v_cvt_f32_ubyte0_e32 v1, v14
	v_cvt_f32_ubyte0_e32 v2, v15
	v_cvt_f32_ubyte1_e32 v16, v14
	v_cvt_f32_ubyte1_e32 v17, v15
	v_cvt_f32_ubyte2_e32 v18, v14
	v_cvt_f32_ubyte2_e32 v19, v15
	v_cvt_f32_ubyte3_e32 v14, v14
	v_cvt_f32_ubyte3_e32 v15, v15
	v_mul_f32_e32 v1, 0x3b808081, v1
	v_mul_f32_e32 v2, 0x3b808081, v2
	v_mul_f32_e32 v16, 0x3b808081, v16
	v_mul_f32_e32 v17, 0x3b808081, v17
	v_mul_f32_e32 v18, 0x3b808081, v18
	v_mul_f32_e32 v19, 0x3b808081, v19
	v_mul_f32_e32 v14, 0x3b808081, v14
	v_mul_f32_e32 v15, 0x3b808081, v15
	v_max_f32_e32 v27, 0x1e3ce508, v1
	v_max_f32_e32 v25, 0x1e3ce508, v16
	v_max_f32_e32 v23, 0x1e3ce508, v18
	v_max_f32_e32 v22, 0x1e3ce508, v14
	v_max_f32_e32 v28, 0x1e3ce508, v2
	v_max_f32_e32 v26, 0x1e3ce508, v17
	v_max_f32_e32 v24, 0x1e3ce508, v19
	v_max_f32_e32 v2, 0x1e3ce508, v15
	s_cbranch_vccz .LBB0_1742
	s_andn2_b64 vcc, exec, s[0:1]
	s_cbranch_vccz .LBB0_1743

.LBB0_1742:
	v_lshl_add_u64 v[14:15], s[8:9], 0, v[4:5]
	v_mov_b32_e32 v14, v236
	v_mov_b32_e32 v15, v237
	v_rcp_f32_e32 v1, v27
	v_rcp_f32_e32 v16, v28
	v_rcp_f32_e32 v17, v25
	v_rcp_f32_e32 v18, v26
	v_rcp_f32_e32 v19, v23
	v_rcp_f32_e32 v20, v24
	v_rcp_f32_e32 v21, v22
	v_rcp_f32_e32 v29, v2
	v_cvt_f32_ubyte0_e32 v46, v14
	v_cvt_f32_ubyte0_e32 v47, v15
	v_cvt_f32_ubyte1_e32 v48, v14
	v_cvt_f32_ubyte1_e32 v49, v15
	v_cvt_f32_ubyte2_e32 v50, v14
	v_cvt_f32_ubyte2_e32 v51, v15
	v_cvt_f32_ubyte3_e32 v14, v14
	v_cvt_f32_ubyte3_e32 v15, v15
	v_mul_f32_e32 v46, 0x3b808081, v46
	v_mul_f32_e32 v47, 0x3b808081, v47
	v_mul_f32_e32 v48, 0x3b808081, v48
	v_mul_f32_e32 v49, 0x3b808081, v49
	v_mul_f32_e32 v50, 0x3b808081, v50
	v_mul_f32_e32 v51, 0x3b808081, v51
	v_mul_f32_e32 v14, 0x3b808081, v14
	v_mul_f32_e32 v15, 0x3b808081, v15
	v_mul_f32_e32 v1, v1, v46
	v_mul_f32_e32 v16, v16, v47
	v_mul_f32_e32 v17, v17, v48
	v_mul_f32_e32 v46, v18, v49
	v_mul_f32_e32 v47, v19, v50
	v_mul_f32_e32 v20, v20, v51
	v_mul_f32_e32 v21, v21, v14
	v_mul_f32_e32 v29, v29, v15
	v_mul_f32_e32 v14, v10, v1
	v_mul_f32_e32 v18, v6, v16
	v_mul_f32_e32 v15, v11, v17
	v_mul_f32_e32 v19, v7, v46
	v_mul_f32_e32 v16, v12, v47
	v_mul_f32_e32 v20, v8, v20
	v_mul_f32_e32 v17, v13, v21
	v_mul_f32_e32 v21, v9, v29
	s_cbranch_execnz .LBB0_1741
